# also the merge GEMM tail round: idle workgroups convert 2 int8 weight blocks each (w_out tails 2 each); prologue keeps 2272 of 4960 wq_single tasks
# speedup vs baseline: 1.0092x; 1.0027x over previous
.LBB0_109:
	v_readlane_b32 s0, v251, 5
	v_readlane_b32 s6, v251, 11
	v_readlane_b32 s7, v251, 12
	s_add_u32 s0, s6, 0x10f00000
	v_writelane_b32 v252, s0, 12
	s_addc_u32 s0, s7, 0
	v_writelane_b32 v252, s0, 13
	s_add_u32 s0, s6, 0x3c90c0
	v_writelane_b32 v252, s0, 14
	s_addc_u32 s0, s7, 0
	v_writelane_b32 v252, s0, 15
	s_add_u32 s0, s6, 0x3ad0c0
	v_writelane_b32 v252, s0, 16
	s_addc_u32 s0, s7, 0
	v_writelane_b32 v252, s0, 17
	s_add_u32 s0, s6, 0x13800000
	v_writelane_b32 v252, s0, 18
	s_addc_u32 s0, s7, 0
	v_writelane_b32 v252, s0, 19
	s_add_u32 s0, s6, 0x33d0c0
	v_writelane_b32 v252, s0, 20
	s_addc_u32 s0, s7, 0
	v_writelane_b32 v252, s0, 21
	s_add_u32 s0, s6, 0x11700000
	v_writelane_b32 v252, s0, 22
	s_addc_u32 s0, s7, 0
	v_writelane_b32 v252, s0, 23
	s_add_u32 s0, s6, 0x3320c0
	v_mov_b32_e32 v0, 0x135f
	v_readlane_b32 s1, v251, 6
	v_writelane_b32 v252, s0, 24
	s_addc_u32 s0, s7, 0
	v_cmp_gt_i32_e32 vcc, s28, v0
	v_readlane_b32 s2, v251, 7
	v_readlane_b32 s3, v251, 8
	v_readlane_b32 s4, v251, 9
	v_readlane_b32 s5, v251, 10
	v_writelane_b32 v252, s0, 25
	s_and_b64 s[0:1], vcc, exec
	s_mov_b64 s[0:1], s[52:53]
	s_mov_b64 s[2:3], s[54:55]
	s_mov_b64 s[4:5], s[56:57]
	s_mov_b64 s[6:7], s[58:59]
	s_mov_b64 s[8:9], s[60:61]
	s_mov_b64 s[10:11], s[62:63]
	s_mov_b64 s[12:13], s[64:65]
	v_writelane_b32 v252, s0, 26
	s_waitcnt lgkmcnt(0)
	s_barrier
	v_writelane_b32 v252, s1, 27
	v_writelane_b32 v252, s2, 28
	v_writelane_b32 v252, s3, 29
	v_writelane_b32 v252, s4, 30
	v_writelane_b32 v252, s5, 31
	v_writelane_b32 v252, s6, 32
	v_writelane_b32 v252, s7, 33
	v_writelane_b32 v252, s8, 34
	v_writelane_b32 v252, s9, 35
	v_writelane_b32 v252, s10, 36
	v_writelane_b32 v252, s11, 37
	v_writelane_b32 v252, s12, 38
	v_writelane_b32 v252, s13, 39
	v_writelane_b32 v252, s14, 40
	v_writelane_b32 v252, s15, 41
	s_cbranch_scc1 .LBB0_253
	s_mov_b32 s98, s28
	v_readlane_b32 s100, v251, 24
	s_movk_i32 s99, 0x8e0
	s_mov_b32 s101, 0
	s_mov_b32 s0, 0xfffff6b0
	s_cmp_lt_u32 s98, 0x11b0
	s_cselect_b32 s0, 0x1b0, s0
	s_cmp_lt_u32 s98, 0x1190
	s_cselect_b32 s0, 0x150, s0
	s_cmp_lt_u32 s98, 0x1180
	s_cselect_b32 s0, 0x150, s0
	s_cmp_lt_u32 s98, 0x10b0
	s_cselect_b32 s0, 0xfffff0b0, s0
	s_cmp_lt_u32 s98, 0x1000
	s_cselect_b32 s0, 0x340, s0
	s_cmp_lt_u32 s98, 0xfe0
	s_cselect_b32 s0, 0xfffff780, s0
	s_cmp_lt_u32 s98, 0xe00
	s_cselect_b32 s0, 0xfffff780, s0
	s_cmp_lt_u32 s98, 0xc60
	s_cselect_b32 s0, 0xfffff780, s0
	s_cmp_lt_u32 s98, 0xa80
	s_cselect_b32 s0, 0xfffff780, s0
	s_cmp_lt_u32 s98, 0x9e0
	s_cselect_b32 s0, 0x940, s0
	s_cmp_lt_u32 s98, 0x9c0
	s_cselect_b32 s0, 0x760, s0
	s_cmp_lt_u32 s98, 0x8e0
	s_cselect_b32 s0, 0x680, s0
	s_cmp_lt_u32 s98, 0x390
	s_cselect_b32 s0, 0xe70, s0
	s_cmp_lt_u32 s98, 0x2b0
	s_cselect_b32 s0, 0x5b0, s0
	s_cmp_lt_u32 s98, 0x1b0
	s_cselect_b32 s0, 0x1150, s0
	s_cmp_lt_u32 s98, 0x190
	s_cselect_b32 s0, 0xeb0, s0
	s_cmp_lt_u32 s98, 0xb0
	s_cselect_b32 s0, 0x0, s0
	s_add_i32 s28, s98, s0
	v_lshlrev_b32_e32 v0, 2, v50
	s_add_i32 s0, 0, 0x21000
	v_and_b32_e32 v37, 31, v50
	v_add_u32_e32 v39, s0, v0
	v_cmp_gt_i32_e64 s[0:1], 32, v50
	v_lshlrev_b32_e32 v1, 1, v50
	v_lshlrev_b32_e32 v42, 2, v37
	v_writelane_b32 v252, s0, 42
	v_ashrrev_i32_e32 v40, 3, v50
	v_and_b32_e32 v2, 0xffffffc0, v1
	v_add_u32_e32 v4, 0, v42
	v_writelane_b32 v252, s1, 43
	s_add_i32 s0, 0, 0x21800
	s_movk_i32 s2, 0x84
	v_and_b32_e32 v45, 7, v50
	v_add_u32_e32 v43, s0, v0
	v_add_u32_e32 v82, s0, v42
	v_mad_u64_u32 v[6:7], s[0:1], v2, s2, v[4:5]
	v_mul_lo_u32 v41, v40, s2
	v_lshlrev_b32_e32 v45, 4, v45
	v_add3_u32 v83, v41, v45, 0
	v_lshrrev_b32_e32 v45, 5, v50
	s_movk_i32 s0, 0x2100
	v_and_b32_e32 v35, 28, v0
	v_or_b32_e32 v0, 62, v1
	v_or_b32_e32 v1, 63, v1
	v_mul_lo_u32 v84, v45, s0
	v_mul_lo_u32 v0, v0, s2
	v_mul_lo_u32 v44, v1, s2
	v_or_b32_e32 v10, 2, v2
	v_or_b32_e32 v12, 4, v2
	v_or_b32_e32 v14, 6, v2
	v_or_b32_e32 v16, 8, v2
	v_or_b32_e32 v18, 10, v2
	v_or_b32_e32 v20, 12, v2
	v_or_b32_e32 v22, 14, v2
	v_or_b32_e32 v24, 16, v2
	v_or_b32_e32 v26, 18, v2
	v_or_b32_e32 v28, 20, v2
	v_or_b32_e32 v30, 22, v2
	v_or_b32_e32 v32, 24, v2
	v_or_b32_e32 v34, 26, v2
	v_or_b32_e32 v36, 28, v2
	v_or_b32_e32 v38, 30, v2
	v_ashrrev_i32_e32 v41, 31, v40
	v_or_b32_e32 v42, v84, v42
	v_ashrrev_i32_e32 v3, 31, v2
	v_mov_b32_e32 v8, v2
	v_mov_b32_e32 v1, v2
	v_mov_b32_e32 v5, v10
	v_mov_b32_e32 v7, v12
	v_mov_b32_e32 v9, v14
	v_mov_b32_e32 v11, v16
	v_mov_b32_e32 v13, v18
	v_mov_b32_e32 v15, v20
	v_mov_b32_e32 v17, v22
	v_mov_b32_e32 v19, v24
	v_mov_b32_e32 v21, v26
	v_mov_b32_e32 v23, v28
	v_mov_b32_e32 v25, v30
	v_mov_b32_e32 v27, v32
	v_mov_b32_e32 v29, v34
	v_mov_b32_e32 v31, v36
	v_mov_b32_e32 v33, v38
	v_lshlrev_b64 v[40:41], 2, v[40:41]
	v_add_u32_e32 v42, 0, v42
	v_mov_b32_e32 v45, 0
	v_add_u32_e32 v85, v4, v0
	v_add_u32_e32 v86, v4, v44
	s_branch .LBB0_112
.LBB0_111:
	s_or_b64 exec, exec, s[0:1]
	s_waitcnt lgkmcnt(0)
	s_barrier
	ds_read_b32 v0, v82
	ds_read_b32 v44, v85
	ds_read_b32 v58, v86
	s_mov_b32 s2, 0x42fe0000
	v_add_u32_e32 v57, 0x400, v6
	s_waitcnt lgkmcnt(2)
	v_div_scale_f32 v46, s[0:1], v0, v0, s2
	v_rcp_f32_e32 v47, v46
	v_readlane_b32 s0, v252, 46
	v_readlane_b32 s1, v252, 47
	v_add_u32_e32 v60, 0x800, v6
	v_fma_f32 v48, -v46, v47, 1.0
	v_fmac_f32_e32 v47, v48, v47
	v_div_scale_f32 v48, vcc, s2, v0, s2
	v_mul_f32_e32 v49, v48, v47
	v_fma_f32 v52, -v46, v49, v48
	v_fmac_f32_e32 v49, v52, v47
	v_fma_f32 v46, -v46, v49, v48
	v_div_fmas_f32 v46, v46, v47, v49
	ds_read2_b32 v[48:49], v6 offset1:33
	v_div_fixup_f32 v46, v46, v0, s2
	v_cmp_lt_f32_e32 vcc, 0, v0
	ds_read2_b32 v[52:53], v6 offset0:66 offset1:99
	v_readlane_b32 s28, v252, 44
	v_cndmask_b32_e32 v0, 0, v46, vcc
	s_waitcnt lgkmcnt(1)
	v_mul_f32_e32 v48, v48, v0
	v_rndne_f32_e32 v48, v48
	v_cvt_i32_f32_e32 v54, v48
	v_mul_f32_e32 v48, v0, v49
	v_rndne_f32_e32 v48, v48
	v_cvt_i32_f32_e32 v55, v48
	s_waitcnt lgkmcnt(0)
	v_mul_f32_e32 v48, v0, v52
	v_rndne_f32_e32 v48, v48
	v_cvt_i32_f32_sdwa v52, v48 dst_sel:WORD_1 dst_unused:UNUSED_PAD src0_sel:DWORD
	v_mul_f32_e32 v48, v0, v53
	v_or_b32_e32 v46, s33, v37
	v_rndne_f32_e32 v48, v48
	v_ashrrev_i32_e32 v47, 31, v46
	v_cvt_i32_f32_sdwa v53, v48 dst_sel:BYTE_3 dst_unused:UNUSED_PAD src0_sel:DWORD
	ds_read2_b32 v[48:49], v6 offset0:132 offset1:165
	v_lshlrev_b64 v[46:47], 10, v[46:47]
	v_lshl_add_u64 v[46:47], s[0:1], 0, v[46:47]
	v_lshlrev_b32_e32 v55, 8, v55
	s_mov_b32 s0, 0xc0c0500
	v_perm_b32 v54, v55, v54, s0
	v_and_b32_e32 v52, 0xff0000, v52
	v_or3_b32 v52, v54, v52, v53
	ds_read2_b32 v[54:55], v6 offset0:198 offset1:231
	s_waitcnt lgkmcnt(1)
	v_mul_f32_e32 v48, v0, v48
	v_rndne_f32_e32 v48, v48
	v_cvt_i32_f32_e32 v53, v48
	v_mul_f32_e32 v48, v0, v49
	v_rndne_f32_e32 v48, v48
	v_cvt_i32_f32_e32 v56, v48
	s_waitcnt lgkmcnt(0)
	v_mul_f32_e32 v48, v0, v54
	v_rndne_f32_e32 v48, v48
	v_cvt_i32_f32_sdwa v54, v48 dst_sel:WORD_1 dst_unused:UNUSED_PAD src0_sel:DWORD
	v_mul_f32_e32 v48, v0, v55
	v_rndne_f32_e32 v48, v48
	v_cvt_i32_f32_sdwa v55, v48 dst_sel:BYTE_3 dst_unused:UNUSED_PAD src0_sel:DWORD
	ds_read2_b32 v[48:49], v57 offset0:8 offset1:41
	v_lshlrev_b32_e32 v56, 8, v56
	v_perm_b32 v53, v56, v53, s0
	v_and_b32_e32 v54, 0xff0000, v54
	v_or3_b32 v53, v53, v54, v55
	ds_read2_b32 v[54:55], v57 offset0:74 offset1:107
	s_waitcnt lgkmcnt(1)
	v_mul_f32_e32 v48, v0, v48
	v_rndne_f32_e32 v48, v48
	v_cvt_i32_f32_e32 v56, v48
	v_mul_f32_e32 v48, v0, v49
	v_rndne_f32_e32 v48, v48
	v_cvt_i32_f32_e32 v59, v48
	s_waitcnt lgkmcnt(0)
	v_mul_f32_e32 v48, v0, v54
	v_rndne_f32_e32 v48, v48
	v_cvt_i32_f32_sdwa v54, v48 dst_sel:WORD_1 dst_unused:UNUSED_PAD src0_sel:DWORD
	v_mul_f32_e32 v48, v0, v55
	v_rndne_f32_e32 v48, v48
	v_cvt_i32_f32_sdwa v55, v48 dst_sel:BYTE_3 dst_unused:UNUSED_PAD src0_sel:DWORD
	ds_read2_b32 v[48:49], v57 offset0:140 offset1:173
	v_lshlrev_b32_e32 v59, 8, v59
	v_perm_b32 v56, v59, v56, s0
	v_and_b32_e32 v54, 0xff0000, v54
	v_or3_b32 v54, v56, v54, v55
	ds_read2_b32 v[56:57], v57 offset0:206 offset1:239
	s_waitcnt lgkmcnt(1)
	v_mul_f32_e32 v48, v0, v48
	v_mul_f32_e32 v49, v0, v49
	v_rndne_f32_e32 v48, v48
	v_rndne_f32_e32 v49, v49
	v_cvt_i32_f32_e32 v55, v48
	s_waitcnt lgkmcnt(0)
	v_mul_f32_e32 v48, v0, v56
	v_cvt_i32_f32_e32 v49, v49
	v_rndne_f32_e32 v48, v48
	v_cvt_i32_f32_sdwa v56, v48 dst_sel:WORD_1 dst_unused:UNUSED_PAD src0_sel:DWORD
	v_mul_f32_e32 v48, v0, v57
	v_rndne_f32_e32 v48, v48
	v_cvt_i32_f32_sdwa v57, v48 dst_sel:BYTE_3 dst_unused:UNUSED_PAD src0_sel:DWORD
	v_lshlrev_b32_e32 v59, 8, v49
	ds_read2_b32 v[48:49], v60 offset0:16 offset1:49
	v_perm_b32 v55, v59, v55, s0
	v_and_b32_e32 v56, 0xff0000, v56
	v_lshl_add_u64 v[46:47], v[46:47], 0, v[2:3]
	v_or3_b32 v55, v55, v56, v57
	global_store_dwordx4 v[46:47], v[52:55], off
	ds_read2_b32 v[52:53], v60 offset0:82 offset1:115
	s_waitcnt lgkmcnt(1)
	v_mul_f32_e32 v48, v0, v48
	v_rndne_f32_e32 v48, v48
	v_cvt_i32_f32_e32 v54, v48
	v_mul_f32_e32 v48, v0, v49
	v_rndne_f32_e32 v48, v48
	v_cvt_i32_f32_e32 v55, v48
	s_waitcnt lgkmcnt(0)
	v_mul_f32_e32 v48, v0, v52
	v_rndne_f32_e32 v48, v48
	v_cvt_i32_f32_sdwa v52, v48 dst_sel:WORD_1 dst_unused:UNUSED_PAD src0_sel:DWORD
	v_mul_f32_e32 v48, v0, v53
	v_rndne_f32_e32 v48, v48
	v_cvt_i32_f32_sdwa v53, v48 dst_sel:BYTE_3 dst_unused:UNUSED_PAD src0_sel:DWORD
	ds_read2_b32 v[48:49], v60 offset0:148 offset1:181
	v_lshlrev_b32_e32 v55, 8, v55
	v_perm_b32 v54, v55, v54, s0
	v_and_b32_e32 v52, 0xff0000, v52
	v_or3_b32 v52, v54, v52, v53
	ds_read2_b32 v[54:55], v60 offset0:214 offset1:247
	s_waitcnt lgkmcnt(1)
	v_mul_f32_e32 v48, v0, v48
	v_rndne_f32_e32 v48, v48
	v_cvt_i32_f32_e32 v53, v48
	v_mul_f32_e32 v48, v0, v49
	v_rndne_f32_e32 v48, v48
	v_cvt_i32_f32_e32 v56, v48
	s_waitcnt lgkmcnt(0)
	v_mul_f32_e32 v48, v0, v54
	v_rndne_f32_e32 v48, v48
	v_cvt_i32_f32_sdwa v54, v48 dst_sel:WORD_1 dst_unused:UNUSED_PAD src0_sel:DWORD
	v_mul_f32_e32 v48, v0, v55
	v_rndne_f32_e32 v48, v48
	v_add_u32_e32 v57, 0xc00, v6
	v_cvt_i32_f32_sdwa v55, v48 dst_sel:BYTE_3 dst_unused:UNUSED_PAD src0_sel:DWORD
	ds_read2_b32 v[48:49], v57 offset0:24 offset1:57
	v_lshlrev_b32_e32 v56, 8, v56
	v_perm_b32 v53, v56, v53, s0
	v_and_b32_e32 v54, 0xff0000, v54
	v_or3_b32 v53, v53, v54, v55
	ds_read2_b32 v[54:55], v57 offset0:90 offset1:123
	s_waitcnt lgkmcnt(1)
	v_mul_f32_e32 v48, v0, v48
	v_rndne_f32_e32 v48, v48
	v_cvt_i32_f32_e32 v56, v48
	v_mul_f32_e32 v48, v0, v49
	v_rndne_f32_e32 v48, v48
	v_cvt_i32_f32_e32 v59, v48
	s_waitcnt lgkmcnt(0)
	v_mul_f32_e32 v48, v0, v54
	v_rndne_f32_e32 v48, v48
	v_cvt_i32_f32_sdwa v54, v48 dst_sel:WORD_1 dst_unused:UNUSED_PAD src0_sel:DWORD
	v_mul_f32_e32 v48, v0, v55
	v_rndne_f32_e32 v48, v48
	v_cvt_i32_f32_sdwa v55, v48 dst_sel:BYTE_3 dst_unused:UNUSED_PAD src0_sel:DWORD
	ds_read2_b32 v[48:49], v57 offset0:156 offset1:189
	v_lshlrev_b32_e32 v59, 8, v59
	v_perm_b32 v56, v59, v56, s0
	v_and_b32_e32 v54, 0xff0000, v54
	v_or3_b32 v54, v56, v54, v55
	ds_read2_b32 v[56:57], v57 offset0:222 offset1:255
	s_waitcnt lgkmcnt(1)
	v_mul_f32_e32 v48, v0, v48
	v_mul_f32_e32 v49, v0, v49
	v_rndne_f32_e32 v48, v48
	v_rndne_f32_e32 v49, v49
	v_cvt_i32_f32_e32 v55, v48
	s_waitcnt lgkmcnt(0)
	v_mul_f32_e32 v48, v0, v56
	v_cvt_i32_f32_e32 v49, v49
	v_rndne_f32_e32 v48, v48
	v_cvt_i32_f32_sdwa v56, v48 dst_sel:WORD_1 dst_unused:UNUSED_PAD src0_sel:DWORD
	v_mul_f32_e32 v48, v0, v57
	v_rndne_f32_e32 v48, v48
	v_cvt_i32_f32_sdwa v57, v48 dst_sel:BYTE_3 dst_unused:UNUSED_PAD src0_sel:DWORD
	v_add_u32_e32 v60, 0x1000, v6
	v_lshlrev_b32_e32 v59, 8, v49
	ds_read2_b32 v[48:49], v60 offset0:32 offset1:65
	v_perm_b32 v55, v59, v55, s0
	v_and_b32_e32 v56, 0xff0000, v56
	v_or3_b32 v55, v55, v56, v57
	global_store_dwordx4 v[46:47], v[52:55], off offset:16
	ds_read2_b32 v[52:53], v60 offset0:98 offset1:131
	s_waitcnt lgkmcnt(1)
	v_mul_f32_e32 v48, v0, v48
	v_rndne_f32_e32 v48, v48
	v_cvt_i32_f32_e32 v54, v48
	v_mul_f32_e32 v48, v0, v49
	v_rndne_f32_e32 v48, v48
	v_cvt_i32_f32_e32 v55, v48
	s_waitcnt lgkmcnt(0)
	v_mul_f32_e32 v48, v0, v52
	v_rndne_f32_e32 v48, v48
	v_cvt_i32_f32_sdwa v52, v48 dst_sel:WORD_1 dst_unused:UNUSED_PAD src0_sel:DWORD
	v_mul_f32_e32 v48, v0, v53
	v_rndne_f32_e32 v48, v48
	v_cvt_i32_f32_sdwa v53, v48 dst_sel:BYTE_3 dst_unused:UNUSED_PAD src0_sel:DWORD
	ds_read2_b32 v[48:49], v60 offset0:164 offset1:197
	v_lshlrev_b32_e32 v55, 8, v55
	v_perm_b32 v54, v55, v54, s0
	v_and_b32_e32 v52, 0xff0000, v52
	v_or3_b32 v52, v54, v52, v53
	v_add_u32_e32 v53, 0x1200, v6
	ds_read2_b32 v[54:55], v53 offset0:102 offset1:135
	s_waitcnt lgkmcnt(1)
	v_mul_f32_e32 v48, v0, v48
	v_rndne_f32_e32 v48, v48
	v_cvt_i32_f32_e32 v53, v48
	v_mul_f32_e32 v48, v0, v49
	v_rndne_f32_e32 v48, v48
	v_cvt_i32_f32_e32 v56, v48
	s_waitcnt lgkmcnt(0)
	v_mul_f32_e32 v48, v0, v54
	v_rndne_f32_e32 v48, v48
	v_cvt_i32_f32_sdwa v54, v48 dst_sel:WORD_1 dst_unused:UNUSED_PAD src0_sel:DWORD
	v_mul_f32_e32 v48, v0, v55
	v_rndne_f32_e32 v48, v48
	v_add_u32_e32 v57, 0x1400, v6
	v_cvt_i32_f32_sdwa v55, v48 dst_sel:BYTE_3 dst_unused:UNUSED_PAD src0_sel:DWORD
	ds_read2_b32 v[48:49], v57 offset0:40 offset1:73
	v_lshlrev_b32_e32 v56, 8, v56
	v_perm_b32 v53, v56, v53, s0
	v_and_b32_e32 v54, 0xff0000, v54
	v_or3_b32 v53, v53, v54, v55
	ds_read2_b32 v[54:55], v57 offset0:106 offset1:139
	s_waitcnt lgkmcnt(1)
	v_mul_f32_e32 v48, v0, v48
	v_rndne_f32_e32 v48, v48
	v_cvt_i32_f32_e32 v56, v48
	v_mul_f32_e32 v48, v0, v49
	v_rndne_f32_e32 v48, v48
	v_cvt_i32_f32_e32 v59, v48
	s_waitcnt lgkmcnt(0)
	v_mul_f32_e32 v48, v0, v54
	v_rndne_f32_e32 v48, v48
	v_cvt_i32_f32_sdwa v54, v48 dst_sel:WORD_1 dst_unused:UNUSED_PAD src0_sel:DWORD
	v_mul_f32_e32 v48, v0, v55
	v_rndne_f32_e32 v48, v48
	v_cvt_i32_f32_sdwa v55, v48 dst_sel:BYTE_3 dst_unused:UNUSED_PAD src0_sel:DWORD
	ds_read2_b32 v[48:49], v57 offset0:172 offset1:205
	v_lshlrev_b32_e32 v57, 8, v59
	v_perm_b32 v56, v57, v56, s0
	v_and_b32_e32 v54, 0xff0000, v54
	v_or3_b32 v54, v56, v54, v55
	v_add_u32_e32 v55, 0x1600, v6
	ds_read2_b32 v[56:57], v55 offset0:110 offset1:143
	s_waitcnt lgkmcnt(1)
	v_mul_f32_e32 v48, v0, v48
	v_mul_f32_e32 v49, v0, v49
	v_rndne_f32_e32 v48, v48
	v_rndne_f32_e32 v49, v49
	v_cvt_i32_f32_e32 v55, v48
	s_waitcnt lgkmcnt(0)
	v_mul_f32_e32 v48, v0, v56
	v_cvt_i32_f32_e32 v49, v49
	v_rndne_f32_e32 v48, v48
	v_cvt_i32_f32_sdwa v56, v48 dst_sel:WORD_1 dst_unused:UNUSED_PAD src0_sel:DWORD
	v_mul_f32_e32 v48, v0, v57
	v_rndne_f32_e32 v48, v48
	v_cvt_i32_f32_sdwa v57, v48 dst_sel:BYTE_3 dst_unused:UNUSED_PAD src0_sel:DWORD
	v_add_u32_e32 v60, 0x1800, v6
	v_lshlrev_b32_e32 v59, 8, v49
	ds_read2_b32 v[48:49], v60 offset0:48 offset1:81
	v_perm_b32 v55, v59, v55, s0
	v_and_b32_e32 v56, 0xff0000, v56
	v_or3_b32 v55, v55, v56, v57
	global_store_dwordx4 v[46:47], v[52:55], off offset:32
	ds_read2_b32 v[52:53], v60 offset0:114 offset1:147
	s_waitcnt lgkmcnt(1)
	v_mul_f32_e32 v48, v0, v48
	v_rndne_f32_e32 v48, v48
	v_cvt_i32_f32_e32 v54, v48
	v_mul_f32_e32 v48, v0, v49
	v_rndne_f32_e32 v48, v48
	v_cvt_i32_f32_e32 v55, v48
	s_waitcnt lgkmcnt(0)
	v_mul_f32_e32 v48, v0, v52
	v_rndne_f32_e32 v48, v48
	v_cvt_i32_f32_sdwa v52, v48 dst_sel:WORD_1 dst_unused:UNUSED_PAD src0_sel:DWORD
	v_mul_f32_e32 v48, v0, v53
	v_rndne_f32_e32 v48, v48
	v_cvt_i32_f32_sdwa v53, v48 dst_sel:BYTE_3 dst_unused:UNUSED_PAD src0_sel:DWORD
	ds_read2_b32 v[48:49], v60 offset0:180 offset1:213
	v_lshlrev_b32_e32 v55, 8, v55
	v_perm_b32 v54, v55, v54, s0
	v_and_b32_e32 v52, 0xff0000, v52
	v_or3_b32 v52, v54, v52, v53
	v_add_u32_e32 v53, 0x1a00, v6
	ds_read2_b32 v[54:55], v53 offset0:118 offset1:151
	s_waitcnt lgkmcnt(1)
	v_mul_f32_e32 v48, v0, v48
	v_rndne_f32_e32 v48, v48
	v_cvt_i32_f32_e32 v53, v48
	v_mul_f32_e32 v48, v0, v49
	v_rndne_f32_e32 v48, v48
	v_cvt_i32_f32_e32 v56, v48
	s_waitcnt lgkmcnt(0)
	v_mul_f32_e32 v48, v0, v54
	v_rndne_f32_e32 v48, v48
	v_cvt_i32_f32_sdwa v54, v48 dst_sel:WORD_1 dst_unused:UNUSED_PAD src0_sel:DWORD
	v_mul_f32_e32 v48, v0, v55
	v_rndne_f32_e32 v48, v48
	v_add_u32_e32 v57, 0x1c00, v6
	v_cvt_i32_f32_sdwa v55, v48 dst_sel:BYTE_3 dst_unused:UNUSED_PAD src0_sel:DWORD
	ds_read2_b32 v[48:49], v57 offset0:56 offset1:89
	v_lshlrev_b32_e32 v56, 8, v56
	v_perm_b32 v53, v56, v53, s0
	v_and_b32_e32 v54, 0xff0000, v54
	v_or3_b32 v53, v53, v54, v55
	ds_read2_b32 v[54:55], v57 offset0:122 offset1:155
	s_waitcnt lgkmcnt(1)
	v_mul_f32_e32 v48, v0, v48
	v_rndne_f32_e32 v48, v48
	v_cvt_i32_f32_e32 v56, v48
	v_mul_f32_e32 v48, v0, v49
	v_rndne_f32_e32 v48, v48
	v_cvt_i32_f32_e32 v59, v48
	s_waitcnt lgkmcnt(0)
	v_mul_f32_e32 v48, v0, v54
	v_rndne_f32_e32 v48, v48
	v_cvt_i32_f32_sdwa v54, v48 dst_sel:WORD_1 dst_unused:UNUSED_PAD src0_sel:DWORD
	v_mul_f32_e32 v48, v0, v55
	v_rndne_f32_e32 v48, v48
	v_cvt_i32_f32_sdwa v55, v48 dst_sel:BYTE_3 dst_unused:UNUSED_PAD src0_sel:DWORD
	ds_read2_b32 v[48:49], v57 offset0:188 offset1:221
	v_mul_f32_e32 v44, v0, v44
	v_rndne_f32_e32 v44, v44
	v_cvt_i32_f32_sdwa v44, v44 dst_sel:WORD_1 dst_unused:UNUSED_PAD src0_sel:DWORD
	v_lshlrev_b32_e32 v57, 8, v59
	s_waitcnt lgkmcnt(0)
	v_mul_f32_e32 v49, v0, v49
	v_mul_f32_e32 v48, v0, v48
	v_rndne_f32_e32 v49, v49
	v_rndne_f32_e32 v48, v48
	v_cvt_i32_f32_e32 v49, v49
	v_cvt_i32_f32_e32 v48, v48
	v_mul_f32_e32 v0, v0, v58
	v_rndne_f32_e32 v0, v0
	v_cvt_i32_f32_sdwa v0, v0 dst_sel:BYTE_3 dst_unused:UNUSED_PAD src0_sel:DWORD
	v_lshlrev_b32_e32 v49, 8, v49
	v_perm_b32 v56, v57, v56, s0
	v_perm_b32 v48, v49, v48, s0
	s_add_i32 s98, s98, s100
	v_and_b32_e32 v54, 0xff0000, v54
	v_and_b32_e32 v44, 0xff0000, v44
	s_mov_b32 s0, 0xfffff6b0
	s_cmp_lt_u32 s98, 0x11b0
	s_cselect_b32 s0, 0x1b0, s0
	s_cmp_lt_u32 s98, 0x1190
	s_cselect_b32 s0, 0x150, s0
	s_cmp_lt_u32 s98, 0x1180
	s_cselect_b32 s0, 0x150, s0
	s_cmp_lt_u32 s98, 0x10b0
	s_cselect_b32 s0, 0xfffff0b0, s0
	s_cmp_lt_u32 s98, 0x1000
	s_cselect_b32 s0, 0x340, s0
	s_cmp_lt_u32 s98, 0xfe0
	s_cselect_b32 s0, 0xfffff780, s0
	s_cmp_lt_u32 s98, 0xe00
	s_cselect_b32 s0, 0xfffff780, s0
	s_cmp_lt_u32 s98, 0xc60
	s_cselect_b32 s0, 0xfffff780, s0
	s_cmp_lt_u32 s98, 0xa80
	s_cselect_b32 s0, 0xfffff780, s0
	s_cmp_lt_u32 s98, 0x9e0
	s_cselect_b32 s0, 0x940, s0
	s_cmp_lt_u32 s98, 0x9c0
	s_cselect_b32 s0, 0x760, s0
	s_cmp_lt_u32 s98, 0x8e0
	s_cselect_b32 s0, 0x680, s0
	s_cmp_lt_u32 s98, 0x390
	s_cselect_b32 s0, 0xe70, s0
	s_cmp_lt_u32 s98, 0x2b0
	s_cselect_b32 s0, 0x5b0, s0
	s_cmp_lt_u32 s98, 0x1b0
	s_cselect_b32 s0, 0x1150, s0
	s_cmp_lt_u32 s98, 0x190
	s_cselect_b32 s0, 0xeb0, s0
	s_cmp_lt_u32 s98, 0xb0
	s_cselect_b32 s0, 0x0, s0
	s_add_i32 s28, s98, s0
	v_or3_b32 v54, v56, v54, v55
	v_or3_b32 v55, v48, v44, v0
	s_cmp_ge_u32 s98, s99
	global_store_dwordx4 v[46:47], v[52:55], off offset:48
	s_barrier
	s_cbranch_scc1 .LBB0_253

.LBB0_1028:
	v_readlane_b32 s98, v251, 3
	v_readlane_b32 s99, v255, 29
	s_cmp_lt_u32 s98, 48
	s_cbranch_scc1 .Lwqd_skip_M
	s_sub_i32 s98, s98, 48
	s_mov_b32 s100, 0
	s_mov_b32 s101, 0
	s_cmp_eq_u32 s99, 0
	s_cselect_b32 s100, 0x8e0, s100
	s_cselect_b32 s101, 0xa80, s101
	s_cmp_eq_u32 s99, 1
	s_cselect_b32 s100, 0xc60, s100
	s_cselect_b32 s101, 0xe00, s101
	s_cmp_eq_u32 s99, 2
	s_cselect_b32 s100, 0xfe0, s100
	s_cselect_b32 s101, 0x1180, s101
	s_add_i32 s98, s98, s100
	s_mov_b32 s99, s101
	s_cmp_ge_u32 s98, s99
	s_cbranch_scc1 .Lwqd_skip_M
	s_movk_i32 s100, 208
	s_mov_b32 s101, 3
	v_writelane_b32 v117, s0, 0
	v_writelane_b32 v117, s1, 1
	v_writelane_b32 v117, s2, 2
	v_writelane_b32 v117, s3, 3
	v_writelane_b32 v117, s4, 4
	v_writelane_b32 v117, s5, 5
	v_writelane_b32 v117, s6, 6
	v_writelane_b32 v117, s7, 7
	v_writelane_b32 v117, s8, 8
	v_writelane_b32 v117, s9, 9
	v_writelane_b32 v117, s10, 10
	v_writelane_b32 v117, s11, 11
	v_writelane_b32 v117, s12, 12
	v_writelane_b32 v117, s13, 13
	v_writelane_b32 v117, s14, 14
	v_writelane_b32 v117, s15, 15
	v_writelane_b32 v117, s16, 16
	v_writelane_b32 v117, s17, 17
	v_writelane_b32 v117, s18, 18
	v_writelane_b32 v117, s19, 19
	v_writelane_b32 v117, s20, 20
	v_writelane_b32 v117, s21, 21
	v_writelane_b32 v117, s22, 22
	v_writelane_b32 v117, s23, 23
	v_writelane_b32 v117, s24, 24
	v_writelane_b32 v117, s25, 25
	v_writelane_b32 v117, s26, 26
	v_writelane_b32 v117, s27, 27
	v_writelane_b32 v117, s28, 28
	v_writelane_b32 v117, s29, 29
	v_writelane_b32 v117, s30, 30
	v_writelane_b32 v117, s31, 31
	v_writelane_b32 v117, s32, 32
	v_writelane_b32 v117, s33, 33
	v_writelane_b32 v117, s34, 34
	v_writelane_b32 v117, s35, 35
	v_writelane_b32 v117, s36, 36
	v_writelane_b32 v117, s37, 37
	v_writelane_b32 v117, s38, 38
	v_writelane_b32 v117, s39, 39
	v_writelane_b32 v117, s40, 40
	v_writelane_b32 v117, s41, 41
	v_writelane_b32 v117, s42, 42
	v_writelane_b32 v117, s43, 43
	v_writelane_b32 v117, s44, 44
	v_writelane_b32 v117, s45, 45
	v_writelane_b32 v117, s46, 46
	v_writelane_b32 v117, s47, 47
	v_writelane_b32 v117, s48, 48
	v_writelane_b32 v117, s49, 49
	v_writelane_b32 v117, s50, 50
	v_writelane_b32 v117, s51, 51
	v_writelane_b32 v117, s52, 52
	v_writelane_b32 v117, s53, 53
	v_writelane_b32 v117, s54, 54
	v_writelane_b32 v117, s55, 55
	v_writelane_b32 v117, s56, 56
	v_writelane_b32 v117, s57, 57
	v_writelane_b32 v117, s58, 58
	v_writelane_b32 v117, s59, 59
	v_writelane_b32 v117, s60, 60
	v_writelane_b32 v117, s61, 61
	v_writelane_b32 v117, s62, 62
	v_writelane_b32 v117, s63, 63
	v_writelane_b32 v118, s64, 0
	v_writelane_b32 v118, s65, 1
	v_writelane_b32 v118, s66, 2
	v_writelane_b32 v118, s67, 3
	v_writelane_b32 v118, s68, 4
	v_writelane_b32 v118, s69, 5
	v_writelane_b32 v118, s70, 6
	v_writelane_b32 v118, s71, 7
	v_writelane_b32 v118, s72, 8
	v_writelane_b32 v118, s73, 9
	v_writelane_b32 v118, s74, 10
	v_writelane_b32 v118, s75, 11
	v_writelane_b32 v118, s76, 12
	v_writelane_b32 v118, s77, 13
	v_writelane_b32 v118, s78, 14
	v_writelane_b32 v118, s79, 15
	v_writelane_b32 v118, s80, 16
	v_writelane_b32 v118, s81, 17
	v_writelane_b32 v118, s82, 18
	v_writelane_b32 v118, s83, 19
	v_writelane_b32 v118, s84, 20
	v_writelane_b32 v118, s85, 21
	v_writelane_b32 v118, s86, 22
	v_writelane_b32 v118, s87, 23
	v_writelane_b32 v118, s88, 24
	v_writelane_b32 v118, s89, 25
	v_writelane_b32 v118, s90, 26
	v_writelane_b32 v118, s91, 27
	v_writelane_b32 v118, s92, 28
	v_writelane_b32 v118, s93, 29
	v_writelane_b32 v118, s94, 30
	v_writelane_b32 v118, s95, 31
	v_writelane_b32 v118, s96, 32
	v_writelane_b32 v118, s97, 33
	v_mov_b32_e32 v100, v0
	v_mov_b32_e32 v101, v50
	v_mov_b32_e32 v102, v51
	v_mov_b32_e32 v103, v52
	v_mov_b32_e32 v104, v54
	v_mov_b32_e32 v105, v55
	v_mov_b32_e32 v106, v56
	v_mov_b32_e32 v107, v58
	v_mov_b32_e32 v108, v59
	v_mov_b32_e32 v109, v60
	v_mov_b32_e32 v110, v62
	v_mov_b32_e32 v111, v63
	v_mov_b32_e32 v112, v64
	v_mov_b32_e32 v113, v67
	v_mov_b32_e32 v114, v75
	v_mov_b32_e32 v115, v77
	s_branch .Lwqd_entry
.Lwqd_ret_M:
	v_mov_b32_e32 v0, v100
	v_mov_b32_e32 v50, v101
	v_mov_b32_e32 v51, v102
	v_mov_b32_e32 v52, v103
	v_mov_b32_e32 v54, v104
	v_mov_b32_e32 v55, v105
	v_mov_b32_e32 v56, v106
	v_mov_b32_e32 v58, v107
	v_mov_b32_e32 v59, v108
	v_mov_b32_e32 v60, v109
	v_mov_b32_e32 v62, v110
	v_mov_b32_e32 v63, v111
	v_mov_b32_e32 v64, v112
	v_mov_b32_e32 v67, v113
	v_mov_b32_e32 v75, v114
	v_mov_b32_e32 v77, v115
	v_readlane_b32 s0, v117, 0
	v_readlane_b32 s1, v117, 1
	v_readlane_b32 s2, v117, 2
	v_readlane_b32 s3, v117, 3
	v_readlane_b32 s4, v117, 4
	v_readlane_b32 s5, v117, 5
	v_readlane_b32 s6, v117, 6
	v_readlane_b32 s7, v117, 7
	v_readlane_b32 s8, v117, 8
	v_readlane_b32 s9, v117, 9
	v_readlane_b32 s10, v117, 10
	v_readlane_b32 s11, v117, 11
	v_readlane_b32 s12, v117, 12
	v_readlane_b32 s13, v117, 13
	v_readlane_b32 s14, v117, 14
	v_readlane_b32 s15, v117, 15
	v_readlane_b32 s16, v117, 16
	v_readlane_b32 s17, v117, 17
	v_readlane_b32 s18, v117, 18
	v_readlane_b32 s19, v117, 19
	v_readlane_b32 s20, v117, 20
	v_readlane_b32 s21, v117, 21
	v_readlane_b32 s22, v117, 22
	v_readlane_b32 s23, v117, 23
	v_readlane_b32 s24, v117, 24
	v_readlane_b32 s25, v117, 25
	v_readlane_b32 s26, v117, 26
	v_readlane_b32 s27, v117, 27
	v_readlane_b32 s28, v117, 28
	v_readlane_b32 s29, v117, 29
	v_readlane_b32 s30, v117, 30
	v_readlane_b32 s31, v117, 31
	v_readlane_b32 s32, v117, 32
	v_readlane_b32 s33, v117, 33
	v_readlane_b32 s34, v117, 34
	v_readlane_b32 s35, v117, 35
	v_readlane_b32 s36, v117, 36
	v_readlane_b32 s37, v117, 37
	v_readlane_b32 s38, v117, 38
	v_readlane_b32 s39, v117, 39
	v_readlane_b32 s40, v117, 40
	v_readlane_b32 s41, v117, 41
	v_readlane_b32 s42, v117, 42
	v_readlane_b32 s43, v117, 43
	v_readlane_b32 s44, v117, 44
	v_readlane_b32 s45, v117, 45
	v_readlane_b32 s46, v117, 46
	v_readlane_b32 s47, v117, 47
	v_readlane_b32 s48, v117, 48
	v_readlane_b32 s49, v117, 49
	v_readlane_b32 s50, v117, 50
	v_readlane_b32 s51, v117, 51
	v_readlane_b32 s52, v117, 52
	v_readlane_b32 s53, v117, 53
	v_readlane_b32 s54, v117, 54
	v_readlane_b32 s55, v117, 55
	v_readlane_b32 s56, v117, 56
	v_readlane_b32 s57, v117, 57
	v_readlane_b32 s58, v117, 58
	v_readlane_b32 s59, v117, 59
	v_readlane_b32 s60, v117, 60
	v_readlane_b32 s61, v117, 61
	v_readlane_b32 s62, v117, 62
	v_readlane_b32 s63, v117, 63
	v_readlane_b32 s64, v118, 0
	v_readlane_b32 s65, v118, 1
	v_readlane_b32 s66, v118, 2
	v_readlane_b32 s67, v118, 3
	v_readlane_b32 s68, v118, 4
	v_readlane_b32 s69, v118, 5
	v_readlane_b32 s70, v118, 6
	v_readlane_b32 s71, v118, 7
	v_readlane_b32 s72, v118, 8
	v_readlane_b32 s73, v118, 9
	v_readlane_b32 s74, v118, 10
	v_readlane_b32 s75, v118, 11
	v_readlane_b32 s76, v118, 12
	v_readlane_b32 s77, v118, 13
	v_readlane_b32 s78, v118, 14
	v_readlane_b32 s79, v118, 15
	v_readlane_b32 s80, v118, 16
	v_readlane_b32 s81, v118, 17
	v_readlane_b32 s82, v118, 18
	v_readlane_b32 s83, v118, 19
	v_readlane_b32 s84, v118, 20
	v_readlane_b32 s85, v118, 21
	v_readlane_b32 s86, v118, 22
	v_readlane_b32 s87, v118, 23
	v_readlane_b32 s88, v118, 24
	v_readlane_b32 s89, v118, 25
	v_readlane_b32 s90, v118, 26
	v_readlane_b32 s91, v118, 27
	v_readlane_b32 s92, v118, 28
	v_readlane_b32 s93, v118, 29
	v_readlane_b32 s94, v118, 30
	v_readlane_b32 s95, v118, 31
	v_readlane_b32 s96, v118, 32
	v_readlane_b32 s97, v118, 33
	s_nop 4
.Lwqd_skip_M:
	s_waitcnt vmcnt(0)
	s_barrier
	s_mov_b64 s[0:1], exec
	v_readlane_b32 s2, v251, 14
	v_readlane_b32 s3, v251, 15
	s_and_b64 s[2:3], s[0:1], s[2:3]
	s_xor_b64 s[0:1], s[2:3], s[0:1]
	s_mov_b64 exec, s[2:3]
	s_cbranch_execz .LBB0_1081
	v_readlane_b32 s2, v255, 9
	s_waitcnt vmcnt(0) expcnt(0) lgkmcnt(0)
	s_nop 0
	v_mov_b32_e32 v1, s2
	ds_read_b32 v3, v1
	v_readlane_b32 s2, v255, 10
	s_waitcnt lgkmcnt(0)
	v_cmp_ne_u32_e32 vcc, 0, v3
	v_mov_b32_e32 v1, s2
	ds_read_b32 v2, v1
	s_cbranch_vccnz .LBB0_1044
	v_readlane_b32 s4, v251, 0
	v_readlane_b32 s5, v251, 1
	s_load_dwordx2 s[2:3], s[4:5], 0x4
	v_readlane_b32 s4, v251, 2
	s_mov_b32 s10, 1
	s_waitcnt lgkmcnt(0)
	s_mul_i32 s8, s2, s4
	s_mul_i32 s8, s8, s3
	s_branch .LBB0_1032

.Lwqd_entry:
	v_mov_b32_e32 v50, v246
	v_mov_b32_e32 v5, 0
	v_readlane_b32 s52, v252, 26
	v_readlane_b32 s53, v252, 27
	s_mov_b32 s0, 0xfffff6b0
	s_cmp_lt_u32 s98, 0x11b0
	s_cselect_b32 s0, 0x1b0, s0
	s_cmp_lt_u32 s98, 0x1190
	s_cselect_b32 s0, 0x150, s0
	s_cmp_lt_u32 s98, 0x1180
	s_cselect_b32 s0, 0x150, s0
	s_cmp_lt_u32 s98, 0x10b0
	s_cselect_b32 s0, 0xfffff0b0, s0
	s_cmp_lt_u32 s98, 0x1000
	s_cselect_b32 s0, 0x340, s0
	s_cmp_lt_u32 s98, 0xfe0
	s_cselect_b32 s0, 0xfffff780, s0
	s_cmp_lt_u32 s98, 0xe00
	s_cselect_b32 s0, 0xfffff780, s0
	s_cmp_lt_u32 s98, 0xc60
	s_cselect_b32 s0, 0xfffff780, s0
	s_cmp_lt_u32 s98, 0xa80
	s_cselect_b32 s0, 0xfffff780, s0
	s_cmp_lt_u32 s98, 0x9e0
	s_cselect_b32 s0, 0x940, s0
	s_cmp_lt_u32 s98, 0x9c0
	s_cselect_b32 s0, 0x760, s0
	s_cmp_lt_u32 s98, 0x8e0
	s_cselect_b32 s0, 0x680, s0
	s_cmp_lt_u32 s98, 0x390
	s_cselect_b32 s0, 0xe70, s0
	s_cmp_lt_u32 s98, 0x2b0
	s_cselect_b32 s0, 0x5b0, s0
	s_cmp_lt_u32 s98, 0x1b0
	s_cselect_b32 s0, 0x1150, s0
	s_cmp_lt_u32 s98, 0x190
	s_cselect_b32 s0, 0xeb0, s0
	s_cmp_lt_u32 s98, 0xb0
	s_cselect_b32 s0, 0x0, s0
	s_add_i32 s28, s98, s0
	v_lshlrev_b32_e32 v0, 2, v50
	s_add_i32 s0, 0, 0x21000
	v_and_b32_e32 v37, 31, v50
	v_add_u32_e32 v39, s0, v0
	v_cmp_gt_i32_e64 s[0:1], 32, v50
	v_lshlrev_b32_e32 v1, 1, v50
	v_lshlrev_b32_e32 v42, 2, v37
	v_writelane_b32 v116, s0, 0
	v_ashrrev_i32_e32 v40, 3, v50
	v_and_b32_e32 v2, 0xffffffc0, v1
	v_add_u32_e32 v4, 0, v42
	v_writelane_b32 v116, s1, 1
	s_add_i32 s0, 0, 0x21800
	s_movk_i32 s2, 0x84
	v_and_b32_e32 v45, 7, v50
	v_add_u32_e32 v43, s0, v0
	v_add_u32_e32 v82, s0, v42
	v_mad_u64_u32 v[6:7], s[0:1], v2, s2, v[4:5]
	v_mul_lo_u32 v41, v40, s2
	v_lshlrev_b32_e32 v45, 4, v45
	v_add3_u32 v83, v41, v45, 0
	v_lshrrev_b32_e32 v45, 5, v50
	s_movk_i32 s0, 0x2100
	v_and_b32_e32 v35, 28, v0
	v_or_b32_e32 v0, 62, v1
	v_or_b32_e32 v1, 63, v1
	v_mul_lo_u32 v84, v45, s0
	v_mul_lo_u32 v0, v0, s2
	v_mul_lo_u32 v44, v1, s2
	v_or_b32_e32 v10, 2, v2
	v_or_b32_e32 v12, 4, v2
	v_or_b32_e32 v14, 6, v2
	v_or_b32_e32 v16, 8, v2
	v_or_b32_e32 v18, 10, v2
	v_or_b32_e32 v20, 12, v2
	v_or_b32_e32 v22, 14, v2
	v_or_b32_e32 v24, 16, v2
	v_or_b32_e32 v26, 18, v2
	v_or_b32_e32 v28, 20, v2
	v_or_b32_e32 v30, 22, v2
	v_or_b32_e32 v32, 24, v2
	v_or_b32_e32 v34, 26, v2
	v_or_b32_e32 v36, 28, v2
	v_or_b32_e32 v38, 30, v2
	v_ashrrev_i32_e32 v41, 31, v40
	v_or_b32_e32 v42, v84, v42
	v_ashrrev_i32_e32 v3, 31, v2
	v_mov_b32_e32 v8, v2
	v_mov_b32_e32 v1, v2
	v_mov_b32_e32 v5, v10
	v_mov_b32_e32 v7, v12
	v_mov_b32_e32 v9, v14
	v_mov_b32_e32 v11, v16
	v_mov_b32_e32 v13, v18
	v_mov_b32_e32 v15, v20
	v_mov_b32_e32 v17, v22
	v_mov_b32_e32 v19, v24
	v_mov_b32_e32 v21, v26
	v_mov_b32_e32 v23, v28
	v_mov_b32_e32 v25, v30
	v_mov_b32_e32 v27, v32
	v_mov_b32_e32 v29, v34
	v_mov_b32_e32 v31, v36
	v_mov_b32_e32 v33, v38
	v_lshlrev_b64 v[40:41], 2, v[40:41]
	v_add_u32_e32 v42, 0, v42
	v_mov_b32_e32 v45, 0
	v_add_u32_e32 v85, v4, v0
	v_add_u32_e32 v86, v4, v44
	s_branch .Lwqd_112
.Lwqd_111:
	s_or_b64 exec, exec, s[0:1]
	s_waitcnt lgkmcnt(0)
	s_barrier
	ds_read_b32 v0, v82
	ds_read_b32 v44, v85
	ds_read_b32 v58, v86
	s_mov_b32 s2, 0x42fe0000
	v_add_u32_e32 v57, 0x400, v6
	s_waitcnt lgkmcnt(2)
	v_div_scale_f32 v46, s[0:1], v0, v0, s2
	v_rcp_f32_e32 v47, v46
	v_readlane_b32 s0, v116, 4
	v_readlane_b32 s1, v116, 5
	v_add_u32_e32 v60, 0x800, v6
	v_fma_f32 v48, -v46, v47, 1.0
	v_fmac_f32_e32 v47, v48, v47
	v_div_scale_f32 v48, vcc, s2, v0, s2
	v_mul_f32_e32 v49, v48, v47
	v_fma_f32 v52, -v46, v49, v48
	v_fmac_f32_e32 v49, v52, v47
	v_fma_f32 v46, -v46, v49, v48
	v_div_fmas_f32 v46, v46, v47, v49
	ds_read2_b32 v[48:49], v6 offset1:33
	v_div_fixup_f32 v46, v46, v0, s2
	v_cmp_lt_f32_e32 vcc, 0, v0
	ds_read2_b32 v[52:53], v6 offset0:66 offset1:99
	v_readlane_b32 s28, v116, 2
	v_cndmask_b32_e32 v0, 0, v46, vcc
	s_waitcnt lgkmcnt(1)
	v_mul_f32_e32 v48, v48, v0
	v_rndne_f32_e32 v48, v48
	v_cvt_i32_f32_e32 v54, v48
	v_mul_f32_e32 v48, v0, v49
	v_rndne_f32_e32 v48, v48
	v_cvt_i32_f32_e32 v55, v48
	s_waitcnt lgkmcnt(0)
	v_mul_f32_e32 v48, v0, v52
	v_rndne_f32_e32 v48, v48
	v_cvt_i32_f32_sdwa v52, v48 dst_sel:WORD_1 dst_unused:UNUSED_PAD src0_sel:DWORD
	v_mul_f32_e32 v48, v0, v53
	v_or_b32_e32 v46, s33, v37
	v_rndne_f32_e32 v48, v48
	v_ashrrev_i32_e32 v47, 31, v46
	v_cvt_i32_f32_sdwa v53, v48 dst_sel:BYTE_3 dst_unused:UNUSED_PAD src0_sel:DWORD
	ds_read2_b32 v[48:49], v6 offset0:132 offset1:165
	v_lshlrev_b64 v[46:47], 10, v[46:47]
	v_lshl_add_u64 v[46:47], s[0:1], 0, v[46:47]
	v_lshlrev_b32_e32 v55, 8, v55
	s_mov_b32 s0, 0xc0c0500
	v_perm_b32 v54, v55, v54, s0
	v_and_b32_e32 v52, 0xff0000, v52
	v_or3_b32 v52, v54, v52, v53
	ds_read2_b32 v[54:55], v6 offset0:198 offset1:231
	s_waitcnt lgkmcnt(1)
	v_mul_f32_e32 v48, v0, v48
	v_rndne_f32_e32 v48, v48
	v_cvt_i32_f32_e32 v53, v48
	v_mul_f32_e32 v48, v0, v49
	v_rndne_f32_e32 v48, v48
	v_cvt_i32_f32_e32 v56, v48
	s_waitcnt lgkmcnt(0)
	v_mul_f32_e32 v48, v0, v54
	v_rndne_f32_e32 v48, v48
	v_cvt_i32_f32_sdwa v54, v48 dst_sel:WORD_1 dst_unused:UNUSED_PAD src0_sel:DWORD
	v_mul_f32_e32 v48, v0, v55
	v_rndne_f32_e32 v48, v48
	v_cvt_i32_f32_sdwa v55, v48 dst_sel:BYTE_3 dst_unused:UNUSED_PAD src0_sel:DWORD
	ds_read2_b32 v[48:49], v57 offset0:8 offset1:41
	v_lshlrev_b32_e32 v56, 8, v56
	v_perm_b32 v53, v56, v53, s0
	v_and_b32_e32 v54, 0xff0000, v54
	v_or3_b32 v53, v53, v54, v55
	ds_read2_b32 v[54:55], v57 offset0:74 offset1:107
	s_waitcnt lgkmcnt(1)
	v_mul_f32_e32 v48, v0, v48
	v_rndne_f32_e32 v48, v48
	v_cvt_i32_f32_e32 v56, v48
	v_mul_f32_e32 v48, v0, v49
	v_rndne_f32_e32 v48, v48
	v_cvt_i32_f32_e32 v59, v48
	s_waitcnt lgkmcnt(0)
	v_mul_f32_e32 v48, v0, v54
	v_rndne_f32_e32 v48, v48
	v_cvt_i32_f32_sdwa v54, v48 dst_sel:WORD_1 dst_unused:UNUSED_PAD src0_sel:DWORD
	v_mul_f32_e32 v48, v0, v55
	v_rndne_f32_e32 v48, v48
	v_cvt_i32_f32_sdwa v55, v48 dst_sel:BYTE_3 dst_unused:UNUSED_PAD src0_sel:DWORD
	ds_read2_b32 v[48:49], v57 offset0:140 offset1:173
	v_lshlrev_b32_e32 v59, 8, v59
	v_perm_b32 v56, v59, v56, s0
	v_and_b32_e32 v54, 0xff0000, v54
	v_or3_b32 v54, v56, v54, v55
	ds_read2_b32 v[56:57], v57 offset0:206 offset1:239
	s_waitcnt lgkmcnt(1)
	v_mul_f32_e32 v48, v0, v48
	v_mul_f32_e32 v49, v0, v49
	v_rndne_f32_e32 v48, v48
	v_rndne_f32_e32 v49, v49
	v_cvt_i32_f32_e32 v55, v48
	s_waitcnt lgkmcnt(0)
	v_mul_f32_e32 v48, v0, v56
	v_cvt_i32_f32_e32 v49, v49
	v_rndne_f32_e32 v48, v48
	v_cvt_i32_f32_sdwa v56, v48 dst_sel:WORD_1 dst_unused:UNUSED_PAD src0_sel:DWORD
	v_mul_f32_e32 v48, v0, v57
	v_rndne_f32_e32 v48, v48
	v_cvt_i32_f32_sdwa v57, v48 dst_sel:BYTE_3 dst_unused:UNUSED_PAD src0_sel:DWORD
	v_lshlrev_b32_e32 v59, 8, v49
	ds_read2_b32 v[48:49], v60 offset0:16 offset1:49
	v_perm_b32 v55, v59, v55, s0
	v_and_b32_e32 v56, 0xff0000, v56
	v_lshl_add_u64 v[46:47], v[46:47], 0, v[2:3]
	v_or3_b32 v55, v55, v56, v57
	global_store_dwordx4 v[46:47], v[52:55], off
	ds_read2_b32 v[52:53], v60 offset0:82 offset1:115
	s_waitcnt lgkmcnt(1)
	v_mul_f32_e32 v48, v0, v48
	v_rndne_f32_e32 v48, v48
	v_cvt_i32_f32_e32 v54, v48
	v_mul_f32_e32 v48, v0, v49
	v_rndne_f32_e32 v48, v48
	v_cvt_i32_f32_e32 v55, v48
	s_waitcnt lgkmcnt(0)
	v_mul_f32_e32 v48, v0, v52
	v_rndne_f32_e32 v48, v48
	v_cvt_i32_f32_sdwa v52, v48 dst_sel:WORD_1 dst_unused:UNUSED_PAD src0_sel:DWORD
	v_mul_f32_e32 v48, v0, v53
	v_rndne_f32_e32 v48, v48
	v_cvt_i32_f32_sdwa v53, v48 dst_sel:BYTE_3 dst_unused:UNUSED_PAD src0_sel:DWORD
	ds_read2_b32 v[48:49], v60 offset0:148 offset1:181
	v_lshlrev_b32_e32 v55, 8, v55
	v_perm_b32 v54, v55, v54, s0
	v_and_b32_e32 v52, 0xff0000, v52
	v_or3_b32 v52, v54, v52, v53
	ds_read2_b32 v[54:55], v60 offset0:214 offset1:247
	s_waitcnt lgkmcnt(1)
	v_mul_f32_e32 v48, v0, v48
	v_rndne_f32_e32 v48, v48
	v_cvt_i32_f32_e32 v53, v48
	v_mul_f32_e32 v48, v0, v49
	v_rndne_f32_e32 v48, v48
	v_cvt_i32_f32_e32 v56, v48
	s_waitcnt lgkmcnt(0)
	v_mul_f32_e32 v48, v0, v54
	v_rndne_f32_e32 v48, v48
	v_cvt_i32_f32_sdwa v54, v48 dst_sel:WORD_1 dst_unused:UNUSED_PAD src0_sel:DWORD
	v_mul_f32_e32 v48, v0, v55
	v_rndne_f32_e32 v48, v48
	v_add_u32_e32 v57, 0xc00, v6
	v_cvt_i32_f32_sdwa v55, v48 dst_sel:BYTE_3 dst_unused:UNUSED_PAD src0_sel:DWORD
	ds_read2_b32 v[48:49], v57 offset0:24 offset1:57
	v_lshlrev_b32_e32 v56, 8, v56
	v_perm_b32 v53, v56, v53, s0
	v_and_b32_e32 v54, 0xff0000, v54
	v_or3_b32 v53, v53, v54, v55
	ds_read2_b32 v[54:55], v57 offset0:90 offset1:123
	s_waitcnt lgkmcnt(1)
	v_mul_f32_e32 v48, v0, v48
	v_rndne_f32_e32 v48, v48
	v_cvt_i32_f32_e32 v56, v48
	v_mul_f32_e32 v48, v0, v49
	v_rndne_f32_e32 v48, v48
	v_cvt_i32_f32_e32 v59, v48
	s_waitcnt lgkmcnt(0)
	v_mul_f32_e32 v48, v0, v54
	v_rndne_f32_e32 v48, v48
	v_cvt_i32_f32_sdwa v54, v48 dst_sel:WORD_1 dst_unused:UNUSED_PAD src0_sel:DWORD
	v_mul_f32_e32 v48, v0, v55
	v_rndne_f32_e32 v48, v48
	v_cvt_i32_f32_sdwa v55, v48 dst_sel:BYTE_3 dst_unused:UNUSED_PAD src0_sel:DWORD
	ds_read2_b32 v[48:49], v57 offset0:156 offset1:189
	v_lshlrev_b32_e32 v59, 8, v59
	v_perm_b32 v56, v59, v56, s0
	v_and_b32_e32 v54, 0xff0000, v54
	v_or3_b32 v54, v56, v54, v55
	ds_read2_b32 v[56:57], v57 offset0:222 offset1:255
	s_waitcnt lgkmcnt(1)
	v_mul_f32_e32 v48, v0, v48
	v_mul_f32_e32 v49, v0, v49
	v_rndne_f32_e32 v48, v48
	v_rndne_f32_e32 v49, v49
	v_cvt_i32_f32_e32 v55, v48
	s_waitcnt lgkmcnt(0)
	v_mul_f32_e32 v48, v0, v56
	v_cvt_i32_f32_e32 v49, v49
	v_rndne_f32_e32 v48, v48
	v_cvt_i32_f32_sdwa v56, v48 dst_sel:WORD_1 dst_unused:UNUSED_PAD src0_sel:DWORD
	v_mul_f32_e32 v48, v0, v57
	v_rndne_f32_e32 v48, v48
	v_cvt_i32_f32_sdwa v57, v48 dst_sel:BYTE_3 dst_unused:UNUSED_PAD src0_sel:DWORD
	v_add_u32_e32 v60, 0x1000, v6
	v_lshlrev_b32_e32 v59, 8, v49
	ds_read2_b32 v[48:49], v60 offset0:32 offset1:65
	v_perm_b32 v55, v59, v55, s0
	v_and_b32_e32 v56, 0xff0000, v56
	v_or3_b32 v55, v55, v56, v57
	global_store_dwordx4 v[46:47], v[52:55], off offset:16
	ds_read2_b32 v[52:53], v60 offset0:98 offset1:131
	s_waitcnt lgkmcnt(1)
	v_mul_f32_e32 v48, v0, v48
	v_rndne_f32_e32 v48, v48
	v_cvt_i32_f32_e32 v54, v48
	v_mul_f32_e32 v48, v0, v49
	v_rndne_f32_e32 v48, v48
	v_cvt_i32_f32_e32 v55, v48
	s_waitcnt lgkmcnt(0)
	v_mul_f32_e32 v48, v0, v52
	v_rndne_f32_e32 v48, v48
	v_cvt_i32_f32_sdwa v52, v48 dst_sel:WORD_1 dst_unused:UNUSED_PAD src0_sel:DWORD
	v_mul_f32_e32 v48, v0, v53
	v_rndne_f32_e32 v48, v48
	v_cvt_i32_f32_sdwa v53, v48 dst_sel:BYTE_3 dst_unused:UNUSED_PAD src0_sel:DWORD
	ds_read2_b32 v[48:49], v60 offset0:164 offset1:197
	v_lshlrev_b32_e32 v55, 8, v55
	v_perm_b32 v54, v55, v54, s0
	v_and_b32_e32 v52, 0xff0000, v52
	v_or3_b32 v52, v54, v52, v53
	v_add_u32_e32 v53, 0x1200, v6
	ds_read2_b32 v[54:55], v53 offset0:102 offset1:135
	s_waitcnt lgkmcnt(1)
	v_mul_f32_e32 v48, v0, v48
	v_rndne_f32_e32 v48, v48
	v_cvt_i32_f32_e32 v53, v48
	v_mul_f32_e32 v48, v0, v49
	v_rndne_f32_e32 v48, v48
	v_cvt_i32_f32_e32 v56, v48
	s_waitcnt lgkmcnt(0)
	v_mul_f32_e32 v48, v0, v54
	v_rndne_f32_e32 v48, v48
	v_cvt_i32_f32_sdwa v54, v48 dst_sel:WORD_1 dst_unused:UNUSED_PAD src0_sel:DWORD
	v_mul_f32_e32 v48, v0, v55
	v_rndne_f32_e32 v48, v48
	v_add_u32_e32 v57, 0x1400, v6
	v_cvt_i32_f32_sdwa v55, v48 dst_sel:BYTE_3 dst_unused:UNUSED_PAD src0_sel:DWORD
	ds_read2_b32 v[48:49], v57 offset0:40 offset1:73
	v_lshlrev_b32_e32 v56, 8, v56
	v_perm_b32 v53, v56, v53, s0
	v_and_b32_e32 v54, 0xff0000, v54
	v_or3_b32 v53, v53, v54, v55
	ds_read2_b32 v[54:55], v57 offset0:106 offset1:139
	s_waitcnt lgkmcnt(1)
	v_mul_f32_e32 v48, v0, v48
	v_rndne_f32_e32 v48, v48
	v_cvt_i32_f32_e32 v56, v48
	v_mul_f32_e32 v48, v0, v49
	v_rndne_f32_e32 v48, v48
	v_cvt_i32_f32_e32 v59, v48
	s_waitcnt lgkmcnt(0)
	v_mul_f32_e32 v48, v0, v54
	v_rndne_f32_e32 v48, v48
	v_cvt_i32_f32_sdwa v54, v48 dst_sel:WORD_1 dst_unused:UNUSED_PAD src0_sel:DWORD
	v_mul_f32_e32 v48, v0, v55
	v_rndne_f32_e32 v48, v48
	v_cvt_i32_f32_sdwa v55, v48 dst_sel:BYTE_3 dst_unused:UNUSED_PAD src0_sel:DWORD
	ds_read2_b32 v[48:49], v57 offset0:172 offset1:205
	v_lshlrev_b32_e32 v57, 8, v59
	v_perm_b32 v56, v57, v56, s0
	v_and_b32_e32 v54, 0xff0000, v54
	v_or3_b32 v54, v56, v54, v55
	v_add_u32_e32 v55, 0x1600, v6
	ds_read2_b32 v[56:57], v55 offset0:110 offset1:143
	s_waitcnt lgkmcnt(1)
	v_mul_f32_e32 v48, v0, v48
	v_mul_f32_e32 v49, v0, v49
	v_rndne_f32_e32 v48, v48
	v_rndne_f32_e32 v49, v49
	v_cvt_i32_f32_e32 v55, v48
	s_waitcnt lgkmcnt(0)
	v_mul_f32_e32 v48, v0, v56
	v_cvt_i32_f32_e32 v49, v49
	v_rndne_f32_e32 v48, v48
	v_cvt_i32_f32_sdwa v56, v48 dst_sel:WORD_1 dst_unused:UNUSED_PAD src0_sel:DWORD
	v_mul_f32_e32 v48, v0, v57
	v_rndne_f32_e32 v48, v48
	v_cvt_i32_f32_sdwa v57, v48 dst_sel:BYTE_3 dst_unused:UNUSED_PAD src0_sel:DWORD
	v_add_u32_e32 v60, 0x1800, v6
	v_lshlrev_b32_e32 v59, 8, v49
	ds_read2_b32 v[48:49], v60 offset0:48 offset1:81
	v_perm_b32 v55, v59, v55, s0
	v_and_b32_e32 v56, 0xff0000, v56
	v_or3_b32 v55, v55, v56, v57
	global_store_dwordx4 v[46:47], v[52:55], off offset:32
	ds_read2_b32 v[52:53], v60 offset0:114 offset1:147
	s_waitcnt lgkmcnt(1)
	v_mul_f32_e32 v48, v0, v48
	v_rndne_f32_e32 v48, v48
	v_cvt_i32_f32_e32 v54, v48
	v_mul_f32_e32 v48, v0, v49
	v_rndne_f32_e32 v48, v48
	v_cvt_i32_f32_e32 v55, v48
	s_waitcnt lgkmcnt(0)
	v_mul_f32_e32 v48, v0, v52
	v_rndne_f32_e32 v48, v48
	v_cvt_i32_f32_sdwa v52, v48 dst_sel:WORD_1 dst_unused:UNUSED_PAD src0_sel:DWORD
	v_mul_f32_e32 v48, v0, v53
	v_rndne_f32_e32 v48, v48
	v_cvt_i32_f32_sdwa v53, v48 dst_sel:BYTE_3 dst_unused:UNUSED_PAD src0_sel:DWORD
	ds_read2_b32 v[48:49], v60 offset0:180 offset1:213
	v_lshlrev_b32_e32 v55, 8, v55
	v_perm_b32 v54, v55, v54, s0
	v_and_b32_e32 v52, 0xff0000, v52
	v_or3_b32 v52, v54, v52, v53
	v_add_u32_e32 v53, 0x1a00, v6
	ds_read2_b32 v[54:55], v53 offset0:118 offset1:151
	s_waitcnt lgkmcnt(1)
	v_mul_f32_e32 v48, v0, v48
	v_rndne_f32_e32 v48, v48
	v_cvt_i32_f32_e32 v53, v48
	v_mul_f32_e32 v48, v0, v49
	v_rndne_f32_e32 v48, v48
	v_cvt_i32_f32_e32 v56, v48
	s_waitcnt lgkmcnt(0)
	v_mul_f32_e32 v48, v0, v54
	v_rndne_f32_e32 v48, v48
	v_cvt_i32_f32_sdwa v54, v48 dst_sel:WORD_1 dst_unused:UNUSED_PAD src0_sel:DWORD
	v_mul_f32_e32 v48, v0, v55
	v_rndne_f32_e32 v48, v48
	v_add_u32_e32 v57, 0x1c00, v6
	v_cvt_i32_f32_sdwa v55, v48 dst_sel:BYTE_3 dst_unused:UNUSED_PAD src0_sel:DWORD
	ds_read2_b32 v[48:49], v57 offset0:56 offset1:89
	v_lshlrev_b32_e32 v56, 8, v56
	v_perm_b32 v53, v56, v53, s0
	v_and_b32_e32 v54, 0xff0000, v54
	v_or3_b32 v53, v53, v54, v55
	ds_read2_b32 v[54:55], v57 offset0:122 offset1:155
	s_waitcnt lgkmcnt(1)
	v_mul_f32_e32 v48, v0, v48
	v_rndne_f32_e32 v48, v48
	v_cvt_i32_f32_e32 v56, v48
	v_mul_f32_e32 v48, v0, v49
	v_rndne_f32_e32 v48, v48
	v_cvt_i32_f32_e32 v59, v48
	s_waitcnt lgkmcnt(0)
	v_mul_f32_e32 v48, v0, v54
	v_rndne_f32_e32 v48, v48
	v_cvt_i32_f32_sdwa v54, v48 dst_sel:WORD_1 dst_unused:UNUSED_PAD src0_sel:DWORD
	v_mul_f32_e32 v48, v0, v55
	v_rndne_f32_e32 v48, v48
	v_cvt_i32_f32_sdwa v55, v48 dst_sel:BYTE_3 dst_unused:UNUSED_PAD src0_sel:DWORD
	ds_read2_b32 v[48:49], v57 offset0:188 offset1:221
	v_mul_f32_e32 v44, v0, v44
	v_rndne_f32_e32 v44, v44
	v_cvt_i32_f32_sdwa v44, v44 dst_sel:WORD_1 dst_unused:UNUSED_PAD src0_sel:DWORD
	v_lshlrev_b32_e32 v57, 8, v59
	s_waitcnt lgkmcnt(0)
	v_mul_f32_e32 v49, v0, v49
	v_mul_f32_e32 v48, v0, v48
	v_rndne_f32_e32 v49, v49
	v_rndne_f32_e32 v48, v48
	v_cvt_i32_f32_e32 v49, v49
	v_cvt_i32_f32_e32 v48, v48
	v_mul_f32_e32 v0, v0, v58
	v_rndne_f32_e32 v0, v0
	v_cvt_i32_f32_sdwa v0, v0 dst_sel:BYTE_3 dst_unused:UNUSED_PAD src0_sel:DWORD
	v_lshlrev_b32_e32 v49, 8, v49
	v_perm_b32 v56, v57, v56, s0
	v_perm_b32 v48, v49, v48, s0
	s_add_i32 s98, s98, s100
	v_and_b32_e32 v54, 0xff0000, v54
	v_and_b32_e32 v44, 0xff0000, v44
	s_mov_b32 s0, 0xfffff6b0
	s_cmp_lt_u32 s98, 0x11b0
	s_cselect_b32 s0, 0x1b0, s0
	s_cmp_lt_u32 s98, 0x1190
	s_cselect_b32 s0, 0x150, s0
	s_cmp_lt_u32 s98, 0x1180
	s_cselect_b32 s0, 0x150, s0
	s_cmp_lt_u32 s98, 0x10b0
	s_cselect_b32 s0, 0xfffff0b0, s0
	s_cmp_lt_u32 s98, 0x1000
	s_cselect_b32 s0, 0x340, s0
	s_cmp_lt_u32 s98, 0xfe0
	s_cselect_b32 s0, 0xfffff780, s0
	s_cmp_lt_u32 s98, 0xe00
	s_cselect_b32 s0, 0xfffff780, s0
	s_cmp_lt_u32 s98, 0xc60
	s_cselect_b32 s0, 0xfffff780, s0
	s_cmp_lt_u32 s98, 0xa80
	s_cselect_b32 s0, 0xfffff780, s0
	s_cmp_lt_u32 s98, 0x9e0
	s_cselect_b32 s0, 0x940, s0
	s_cmp_lt_u32 s98, 0x9c0
	s_cselect_b32 s0, 0x760, s0
	s_cmp_lt_u32 s98, 0x8e0
	s_cselect_b32 s0, 0x680, s0
	s_cmp_lt_u32 s98, 0x390
	s_cselect_b32 s0, 0xe70, s0
	s_cmp_lt_u32 s98, 0x2b0
	s_cselect_b32 s0, 0x5b0, s0
	s_cmp_lt_u32 s98, 0x1b0
	s_cselect_b32 s0, 0x1150, s0
	s_cmp_lt_u32 s98, 0x190
	s_cselect_b32 s0, 0xeb0, s0
	s_cmp_lt_u32 s98, 0xb0
	s_cselect_b32 s0, 0x0, s0
	s_add_i32 s28, s98, s0
	v_or3_b32 v54, v56, v54, v55
	v_or3_b32 v55, v48, v44, v0
	s_cmp_ge_u32 s98, s99
	global_store_dwordx4 v[46:47], v[52:55], off offset:48
	s_barrier
	s_cbranch_scc1 .Lwqd_exit

.Lwqd_exit:
	s_mov_b64 exec, -1
	s_cmp_eq_u32 s101, 1
	s_cbranch_scc1 .Lwqd_ret_A
	s_cmp_eq_u32 s101, 2
	s_branch .Lwqd_ret_M

.LBB0_1159:
	v_readlane_b32 s98, v251, 3
	v_readlane_b32 s99, v255, 29
	s_cmp_lt_u32 s98, 16
	s_cbranch_scc1 .Lwqd_skip_A
	s_sub_i32 s98, s98, 16
	s_mov_b32 s100, 0
	s_mov_b32 s101, 0
	s_cmp_eq_u32 s99, 0
	s_cselect_b32 s100, 0xa80, s100
	s_cselect_b32 s101, 0xc60, s101
	s_cmp_eq_u32 s99, 1
	s_cselect_b32 s100, 0xe00, s100
	s_cselect_b32 s101, 0xfe0, s101
	s_cmp_eq_u32 s99, 2
	s_cselect_b32 s100, 0x1180, s100
	s_cselect_b32 s101, 0x1360, s101
	s_add_i32 s98, s98, s100
	s_mov_b32 s99, s101
	s_cmp_ge_u32 s98, s99
	s_cbranch_scc1 .Lwqd_skip_A
	s_movk_i32 s100, 240
	s_mov_b32 s101, 1
	v_writelane_b32 v117, s0, 0
	v_writelane_b32 v117, s1, 1
	v_writelane_b32 v117, s2, 2
	v_writelane_b32 v117, s3, 3
	v_writelane_b32 v117, s4, 4
	v_writelane_b32 v117, s5, 5
	v_writelane_b32 v117, s6, 6
	v_writelane_b32 v117, s7, 7
	v_writelane_b32 v117, s8, 8
	v_writelane_b32 v117, s9, 9
	v_writelane_b32 v117, s10, 10
	v_writelane_b32 v117, s11, 11
	v_writelane_b32 v117, s12, 12
	v_writelane_b32 v117, s13, 13
	v_writelane_b32 v117, s14, 14
	v_writelane_b32 v117, s15, 15
	v_writelane_b32 v117, s16, 16
	v_writelane_b32 v117, s17, 17
	v_writelane_b32 v117, s18, 18
	v_writelane_b32 v117, s19, 19
	v_writelane_b32 v117, s20, 20
	v_writelane_b32 v117, s21, 21
	v_writelane_b32 v117, s22, 22
	v_writelane_b32 v117, s23, 23
	v_writelane_b32 v117, s24, 24
	v_writelane_b32 v117, s25, 25
	v_writelane_b32 v117, s26, 26
	v_writelane_b32 v117, s27, 27
	v_writelane_b32 v117, s28, 28
	v_writelane_b32 v117, s29, 29
	v_writelane_b32 v117, s30, 30
	v_writelane_b32 v117, s31, 31
	v_writelane_b32 v117, s32, 32
	v_writelane_b32 v117, s33, 33
	v_writelane_b32 v117, s34, 34
	v_writelane_b32 v117, s35, 35
	v_writelane_b32 v117, s36, 36
	v_writelane_b32 v117, s37, 37
	v_writelane_b32 v117, s38, 38
	v_writelane_b32 v117, s39, 39
	v_writelane_b32 v117, s40, 40
	v_writelane_b32 v117, s41, 41
	v_writelane_b32 v117, s42, 42
	v_writelane_b32 v117, s43, 43
	v_writelane_b32 v117, s44, 44
	v_writelane_b32 v117, s45, 45
	v_writelane_b32 v117, s46, 46
	v_writelane_b32 v117, s47, 47
	v_writelane_b32 v117, s48, 48
	v_writelane_b32 v117, s49, 49
	v_writelane_b32 v117, s50, 50
	v_writelane_b32 v117, s51, 51
	v_writelane_b32 v117, s52, 52
	v_writelane_b32 v117, s53, 53
	v_writelane_b32 v117, s54, 54
	v_writelane_b32 v117, s55, 55
	v_writelane_b32 v117, s56, 56
	v_writelane_b32 v117, s57, 57
	v_writelane_b32 v117, s58, 58
	v_writelane_b32 v117, s59, 59
	v_writelane_b32 v117, s60, 60
	v_writelane_b32 v117, s61, 61
	v_writelane_b32 v117, s62, 62
	v_writelane_b32 v117, s63, 63
	v_writelane_b32 v118, s64, 0
	v_writelane_b32 v118, s65, 1
	v_writelane_b32 v118, s66, 2
	v_writelane_b32 v118, s67, 3
	v_writelane_b32 v118, s68, 4
	v_writelane_b32 v118, s69, 5
	v_writelane_b32 v118, s70, 6
	v_writelane_b32 v118, s71, 7
	v_writelane_b32 v118, s72, 8
	v_writelane_b32 v118, s73, 9
	v_writelane_b32 v118, s74, 10
	v_writelane_b32 v118, s75, 11
	v_writelane_b32 v118, s76, 12
	v_writelane_b32 v118, s77, 13
	v_writelane_b32 v118, s78, 14
	v_writelane_b32 v118, s79, 15
	v_writelane_b32 v118, s80, 16
	v_writelane_b32 v118, s81, 17
	v_writelane_b32 v118, s82, 18
	v_writelane_b32 v118, s83, 19
	v_writelane_b32 v118, s84, 20
	v_writelane_b32 v118, s85, 21
	v_writelane_b32 v118, s86, 22
	v_writelane_b32 v118, s87, 23
	v_writelane_b32 v118, s88, 24
	v_writelane_b32 v118, s89, 25
	v_writelane_b32 v118, s90, 26
	v_writelane_b32 v118, s91, 27
	v_writelane_b32 v118, s92, 28
	v_writelane_b32 v118, s93, 29
	v_writelane_b32 v118, s94, 30
	v_writelane_b32 v118, s95, 31
	v_writelane_b32 v118, s96, 32
	v_writelane_b32 v118, s97, 33
	v_mov_b32_e32 v100, v0
	v_mov_b32_e32 v101, v50
	v_mov_b32_e32 v102, v51
	v_mov_b32_e32 v103, v52
	v_mov_b32_e32 v104, v54
	v_mov_b32_e32 v105, v55
	v_mov_b32_e32 v106, v56
	v_mov_b32_e32 v107, v58
	v_mov_b32_e32 v108, v59
	v_mov_b32_e32 v109, v60
	v_mov_b32_e32 v110, v62
	v_mov_b32_e32 v111, v63
	v_mov_b32_e32 v112, v64
	v_mov_b32_e32 v113, v67
	v_mov_b32_e32 v114, v75
	v_mov_b32_e32 v115, v77
	s_branch .Lwqd_entry
